# stack6 + the per-wave sink value of the windowed attention kept in its register across units (reloaded only after a conversion slot)
# speedup vs baseline: 1.0150x; 1.0115x over previous
; #define ATT_BAR() do { asm volatile("s_waitcnt lgkmcnt(0)" ::: "memory"); __builtin_amdgcn_s_barrier(); asm volatile("" ::: "memory"); } while (0)
; #define ATT_DMA(j, slot) ATT_DMA_S(S, j, slot)
; #define ATT_DMA(j, slot) ATT_DMA_S(S, j, slot)
; #define ATT_DMA(j, slot) ATT_DMA_S(S, j, slot)
; __device__ __forceinline__ void unit_swa(const P& p, LAS unsigned char* lds, const Src& S, const int qa  , const float sinkp, bf16_t* orow, const int wid,
;                                          bf16x8 (&qr)[4], const bool pre, const bool pn, const Src& Sn) {
;     ...
;     if (!pre) {
; #pragma unroll
;         for (int d0 = 0; d0 < 4; ++d0) qr[d0] = *(const bf16x8*)(S.q + (size_t)r32 * 64 + d0 * 16 + hi * 8);
;         ATT_DMA(0, 0); ATT_DMA(1, SLOTB); }
; __device__ __forceinline__ void phase(const P& p, LAS unsigned char* lds, int G, int vcu, const int wid) {
;     ...
;     for (int U = vcu; U < NB * 2 * 32 * 2; U += G) {
;         if (iter++ == cslot) { ATT_BAR(); f8_share(p, lds, G, vcu, wid); ATT_BAR(); }
;         ATT_SWA_SRC(U, S, hq, tok0, b);
;         const int Un = U + G; const bool pn = Un < NB * 2 * 32 * 2 && iter != cslot;
;         ATT_SWA_SRC(pn ? Un : U, Sn, hqn, tok0n, bn);
;         unit_swa(p, lds, S, tok0, exp2f(p.sink[hq] * LOG2E), MX + ((size_t)b * SEQ + tok0) * DM + hq * 64, wid, qra, pre, pn, Sn);
.LBB7_485:
	s_ashr_i32 s36, s41, 6
	s_lshl_b32 s9, s41, 1
	s_and_b32 s6, s36, 1
	s_and_b32 s9, s9, 2
	s_bfe_u32 s1, s41, 0x50001
	s_lshl_b32 s8, s6, 2
	s_add_i32 s9, s9, s33
	s_add_i32 s8, s9, s8
	s_lshl_b32 s9, s1, 7
	s_lshl_b32 s11, s1, 1
	s_xor_b64 s[56:57], s[44:45], -1
	s_ashr_i32 s0, s41, 7
	s_or_b32 s9, s9, s34
	s_add_i32 s37, s11, -2
	s_cmp_lg_u32 s1, 0
	s_cselect_b32 s44, s37, 0
	s_add_i32 s11, s11, 3
	s_cmp_lg_u32 s1, 31
	s_cselect_b32 s54, s11, 63
	s_ashr_i32 s37, s36, 31
	s_lshl_b64 s[36:37], s[36:37], 19
	s_add_u32 s1, s13, s36
	s_addc_u32 s11, s81, s37
	s_add_u32 s36, s82, s36
	s_addc_u32 s37, s84, s37
	s_lshl_b32 s6, s6, 13
	s_add_u32 s38, s79, s6
	s_addc_u32 s48, s80, 0
	s_add_u32 s49, s38, 0x4000
	s_addc_u32 s50, s48, 0
	s_lshl_b32 s6, s8, 2
	v_readlane_b32 s60, v254, 25
	s_waitcnt vmcnt(0)
	v_mov_b32_e32 v0, s6
	v_readlane_b32 s61, v254, 26
	v_readlane_b32 s6, v254, 5
	s_sub_i32 s51, s54, s44
	s_mov_b64 s[46:47], -1
	s_and_b64 vcc, exec, s[56:57]
	v_readlane_b32 s62, v254, 27
	s_cbranch_vccz .Lswa_sink_keep
	global_load_dword v111, v0, s[60:61]
.Lswa_sink_keep:
	v_mov_b32_e32 v0, v145
	v_readlane_b32 s63, v254, 28
	v_mbcnt_lo_u32_b32 v0, -1, v0
	v_mbcnt_hi_u32_b32 v108, -1, v0
	v_add_u32_e32 v0, s6, v108
	v_ashrrev_i32_e32 v109, 5, v108
	v_and_b32_e32 v110, 31, v108
	v_lshlrev_b32_e32 v104, 3, v109
	v_lshlrev_b32_e32 v0, 3, v0
	v_lshlrev_b32_e32 v144, 7, v110
	v_ashrrev_i32_e32 v105, 31, v104
	v_ashrrev_i32_e32 v1, 31, v0
	v_readlane_b32 s64, v254, 29
	v_readlane_b32 s65, v254, 30
	v_readlane_b32 s66, v254, 31
	v_readlane_b32 s67, v254, 32
	v_readlane_b32 s68, v254, 33
	v_readlane_b32 s69, v254, 34
	v_readlane_b32 s70, v254, 35
	v_readlane_b32 s71, v254, 36
	v_readlane_b32 s72, v254, 37
	v_readlane_b32 s73, v254, 38
	v_readlane_b32 s74, v254, 39
	v_readlane_b32 s75, v254, 40
	s_cbranch_vccz .LBB7_487
	s_lshl_b32 s6, s0, 3
	s_add_i32 s46, s8, s6
	s_ashr_i32 s47, s46, 31
	s_lshl_b64 s[46:47], s[46:47], 19
	s_add_u32 s6, s5, s46
	s_addc_u32 s45, s12, s47
	s_lshl_b32 s46, s9, 7
	s_add_u32 s46, s6, s46
	s_addc_u32 s47, s45, 0
	s_ashr_i32 s45, s44, 31
	v_lshl_add_u64 v[2:3], s[46:47], 0, v[144:145]
	s_lshl_b64 s[46:47], s[44:45], 13
	s_add_u32 s6, s1, s46
	s_addc_u32 s45, s11, s47
	s_add_u32 s55, s36, s46
	s_addc_u32 s56, s37, s47
	v_lshl_add_u64 v[2:3], v[104:105], 1, v[2:3]
	s_cmp_gt_i32 s51, -1
	global_load_dwordx4 v[64:67], v[2:3], off
	global_load_dwordx4 v[68:71], v[2:3], off offset:32
	global_load_dwordx4 v[72:75], v[2:3], off offset:64
	global_load_dwordx4 v[76:79], v[2:3], off offset:96
	s_cselect_b32 s47, s45, s48
	s_cselect_b32 s46, s6, s38
	v_lshlrev_b64 v[2:3], 1, v[0:1]
	s_cselect_b32 s57, s56, s50
	s_cselect_b32 s56, s55, s49
	s_waitcnt lgkmcnt(0)
	v_lshl_add_u64 v[4:5], s[46:47], 0, v[2:3]
	s_or_b32 s46, s44, 1
	s_ashr_i32 s47, s46, 31
	s_lshl_b64 s[46:47], s[46:47], 13
	s_add_u32 s6, s1, s46
	s_addc_u32 s45, s11, s47
	s_mov_b32 m0, s35
	s_add_u32 s55, s36, s46
	global_load_lds_dwordx4 v[4:5], off
	v_lshl_add_u64 v[4:5], s[56:57], 0, v[2:3]
	s_addc_u32 s56, s37, s47
	s_cmp_gt_i32 s51, 0
	s_mov_b32 m0, s10
	s_cselect_b32 s47, s45, s48
	s_cselect_b32 s46, s6, s38
	global_load_lds_dwordx4 v[4:5], off
	s_cselect_b32 s57, s56, s50
	s_cselect_b32 s56, s55, s49
	v_lshl_add_u64 v[4:5], s[46:47], 0, v[2:3]
	s_add_i32 m0, s35, 0x4000
	v_lshl_add_u64 v[2:3], s[56:57], 0, v[2:3]
	global_load_lds_dwordx4 v[4:5], off
	s_add_i32 m0, s35, 0x6000
	s_mov_b64 s[46:47], 0
	global_load_lds_dwordx4 v[2:3], off
